# baseline (speedup 1.0000x reference)
.LBB2_3:
	s_add_i32 s8, s10, 1
	s_cmp_lg_u32 s8, 2
	s_cselect_b32 s10, s8, 0
	s_add_i32 s4, s4, 64
	s_cmp_eq_u32 s7, s11
	s_cbranch_scc1 .LBB2_8
	.p2align	6

.LBB3_3:
	s_add_i32 s3, s3, 1
	s_cmp_lg_u32 s3, 3
	s_cselect_b32 s3, s3, 0
	s_add_i32 s15, s15, 1
	s_add_i32 s10, s10, 64
	s_cmp_eq_u32 s14, s15
	s_cbranch_scc1 .LBB3_8
	.p2align	6
